# expert GEMMs use the unscaled f8f6f4 MFMA form (unit scales dropped, no v_mfma_ld_scale prefix); bf16 GEMM LDS layout; all previous edits
# speedup vs baseline: 1.0037x; 1.0037x over previous
.LBB0_910:
	s_add_u32 s25, s36, 0x100
	s_addc_u32 s27, s37, 0
	s_lshl_b32 s7, s55, 10
	s_add_i32 s7, s7, 0x24000
	s_mov_b32 s42, -2
	s_mov_b64 s[36:37], 0
	s_cmp_eq_u32 s42, 12
	s_cselect_b64 s[40:41], -1, 0
	s_and_b64 s[38:39], s[34:35], s[40:41]
	s_andn2_b64 vcc, exec, s[38:39]
	v_mov_b32_e32 v128, v186
	v_mov_b32_e32 v129, v176
	s_add_u32 s76, s10, s36
	v_add_u32_e32 v134, s67, v194
	v_add_u32_e32 v142, s67, v195
	v_add_u32_e32 v150, s68, v194
	v_add_u32_e32 v158, s68, v195
	s_addc_u32 s77, s11, s37
	ds_read_b128 v[130:133], v134
	ds_read_b128 v[138:141], v134 offset:2048
	ds_read_b128 v[134:137], v142
	ds_read_b128 v[142:145], v142 offset:2048
	ds_read_b128 v[146:149], v150
	ds_read_b128 v[154:157], v150 offset:2048
	ds_read_b128 v[150:153], v158
	ds_read_b128 v[158:161], v158 offset:2048
	s_add_u32 s43, s76, 0x36000100
	s_addc_u32 s75, s77, 0
	s_and_b64 s[38:39], s[40:41], exec
	s_cselect_b32 s39, s13, s75
	s_cselect_b32 s38, s12, s43
	s_add_u32 s43, s25, s36
	s_addc_u32 s75, s27, s37
	s_and_b64 s[40:41], s[40:41], exec
	s_cselect_b32 s41, s31, s75
	s_cselect_b32 s40, s30, s43
	ds_read_b128 v[162:165], v227
	ds_read_b128 v[232:235], v227 offset:2048
	ds_read_b128 v[166:169], v228
	ds_read_b128 v[236:239], v228 offset:2048
	ds_read_b128 v[240:243], v227 offset:4096
	ds_read_b128 v[196:199], v227 offset:6144
	ds_read_b128 v[244:247], v228 offset:4096
	ds_read_b128 v[200:203], v228 offset:6144
	s_add_i32 m0, s50, 0xc000
	v_lshl_add_u64 v[170:171], s[76:77], 0, v[176:177]
	v_lshl_add_u64 v[170:171], v[170:171], 0, s[16:17]
	v_mov_b32_e32 v187, v177
	global_load_lds_dwordx4 v[170:171], off
	s_add_i32 m0, s50, 0xe000
	v_lshl_add_u64 v[170:171], s[76:77], 0, v[186:187]
	v_lshl_add_u64 v[170:171], v[170:171], 0, s[16:17]
	global_load_lds_dwordx4 v[170:171], off
	s_waitcnt vmcnt(8)
	s_waitcnt lgkmcnt(0)
	s_barrier
	s_setprio 1
	s_waitcnt lgkmcnt(0)
	v_mfma_f32_16x16x128_f8f6f4 v[100:103], v[130:137], v[162:169], 0
	v_mfma_f32_16x16x128_f8f6f4 v[96:99], v[138:145], v[162:169], 0
	v_mfma_f32_16x16x128_f8f6f4 v[92:95], v[130:137], v[232:239], 0
	v_mfma_f32_16x16x128_f8f6f4 v[88:91], v[138:145], v[232:239], 0
	v_mfma_f32_16x16x128_f8f6f4 v[84:87], v[130:137], v[240:247], 0
	v_mfma_f32_16x16x128_f8f6f4 v[80:83], v[138:145], v[240:247], 0
	v_mfma_f32_16x16x128_f8f6f4 v[170:173], v[130:137], v[196:203], 0
	v_mfma_f32_16x16x128_f8f6f4 v[188:191], v[138:145], v[196:203], 0
	s_setprio 0
	s_setprio 1
	v_mfma_f32_16x16x128_f8f6f4 v[40:43], v[146:153], v[196:203], 0
	v_mfma_f32_16x16x128_f8f6f4 v[32:35], v[154:161], v[196:203], 0
	v_mfma_f32_16x16x128_f8f6f4 v[248:251], v[146:153], v[162:169], 0
	v_mfma_f32_16x16x128_f8f6f4 v[204:207], v[154:161], v[162:169], 0
	v_mfma_f32_16x16x128_f8f6f4 v[208:211], v[146:153], v[232:239], 0
	v_mfma_f32_16x16x128_f8f6f4 v[212:215], v[154:161], v[232:239], 0
	v_mfma_f32_16x16x128_f8f6f4 v[216:219], v[146:153], v[240:247], 0
	v_mfma_f32_16x16x128_f8f6f4 v[240:243], v[154:161], v[240:247], 0
	s_setprio 0
	s_barrier
	s_add_i32 s43, s67, s5
	s_mov_b32 m0, s43
	s_nop 2
	ds_read_b128 v[48:51], v227 offset:16384
	ds_read_b128 v[56:59], v227 offset:18432
	ds_read_b128 v[52:55], v228 offset:16384
	ds_read_b128 v[60:63], v228 offset:18432
	ds_read_b128 v[64:67], v227 offset:20480
	ds_read_b128 v[72:75], v227 offset:22528
	ds_read_b128 v[68:71], v228 offset:20480
	ds_read_b128 v[76:79], v228 offset:22528
	s_nop 0
	global_load_lds_dwordx4 v184, s[40:41]
	s_add_i32 m0, s43, 0x2000
	s_add_u32 s76, s40, 0x4000
	s_addc_u32 s77, s41, 0
	s_add_i32 s43, s68, s5
	s_nop 0
	global_load_lds_dwordx4 v178, s[40:41]
	s_mov_b32 m0, s43
	s_nop 0
	global_load_lds_dwordx4 v184, s[76:77]
	s_add_i32 m0, s43, 0x2000
	s_nop 0
	global_load_lds_dwordx4 v178, s[76:77]
	s_waitcnt vmcnt(6)
	s_waitcnt lgkmcnt(0)
	s_barrier
	s_setprio 1
	s_waitcnt lgkmcnt(0)
	v_mfma_f32_16x16x128_f8f6f4 v[44:47], v[130:137], v[48:55], 0
	v_mfma_f32_16x16x128_f8f6f4 v[36:39], v[138:145], v[48:55], 0
	v_mfma_f32_16x16x128_f8f6f4 v[28:31], v[130:137], v[56:63], 0
	v_mfma_f32_16x16x128_f8f6f4 v[24:27], v[138:145], v[56:63], 0
	v_mfma_f32_16x16x128_f8f6f4 v[20:23], v[130:137], v[64:71], 0
	v_mfma_f32_16x16x128_f8f6f4 v[16:19], v[138:145], v[64:71], 0
	v_mfma_f32_16x16x128_f8f6f4 v[12:15], v[130:137], v[72:79], 0
	v_mfma_f32_16x16x128_f8f6f4 v[8:11], v[138:145], v[72:79], 0
	s_setprio 0
	s_setprio 1
	v_mfma_f32_16x16x128_f8f6f4 v[4:7], v[146:153], v[48:55], 0
	v_mfma_f32_16x16x128_f8f6f4 v[0:3], v[154:161], v[48:55], 0
	v_mfma_f32_16x16x128_f8f6f4 v[104:107], v[146:153], v[56:63], 0
	v_mfma_f32_16x16x128_f8f6f4 v[108:111], v[154:161], v[56:63], 0
	v_mfma_f32_16x16x128_f8f6f4 v[112:115], v[146:153], v[64:71], 0
	v_mfma_f32_16x16x128_f8f6f4 v[116:119], v[154:161], v[64:71], 0
	v_mfma_f32_16x16x128_f8f6f4 v[120:123], v[146:153], v[72:79], 0
	v_mfma_f32_16x16x128_f8f6f4 v[124:127], v[154:161], v[72:79], 0
	s_setprio 0
	s_barrier
	s_add_i32 s43, 0, 0x18000
	v_add_u32_e32 v48, s43, v194
	s_add_i32 s75, 0, 0x1c000
	v_add_u32_e32 v49, s43, v195
	ds_read_b128 v[130:133], v48
	ds_read_b128 v[138:141], v48 offset:2048
	ds_read_b128 v[134:137], v49
	ds_read_b128 v[142:145], v49 offset:2048
	v_add_u32_e32 v48, s75, v194
	v_add_u32_e32 v49, s75, v195
	ds_read_b128 v[146:149], v48
	ds_read_b128 v[154:157], v48 offset:2048
	ds_read_b128 v[150:153], v49
	ds_read_b128 v[158:161], v49 offset:2048
	s_mov_b32 m0, s52
	v_mov_b32_e32 v176, v129
	ds_read_b128 v[48:51], v227 offset:32768
	ds_read_b128 v[162:165], v227 offset:34816
	ds_read_b128 v[52:55], v228 offset:32768
	ds_read_b128 v[166:169], v228 offset:34816
	ds_read_b128 v[196:199], v227 offset:36864
	ds_read_b128 v[232:235], v227 offset:38912
	ds_read_b128 v[200:203], v228 offset:36864
	ds_read_b128 v[236:239], v228 offset:38912
	s_mov_b32 m0, s50
	s_nop 0
	global_load_lds_dwordx4 v180, s[38:39]
	s_mov_b32 m0, s51
	s_nop 0
	global_load_lds_dwordx4 v182, s[38:39]
	s_mov_b32 m0, s52
	v_mov_b32_e32 v186, v128
	global_load_lds_dwordx4 v176, s[38:39]
	s_mov_b32 m0, s53
	s_nop 0
	global_load_lds_dwordx4 v186, s[38:39]
	s_waitcnt vmcnt(8)
	s_waitcnt lgkmcnt(0)
	s_barrier
	s_setprio 1
	s_waitcnt lgkmcnt(0)
	v_mfma_f32_16x16x128_f8f6f4 v[100:103], v[130:137], v[48:55], v[100:103]
	v_mfma_f32_16x16x128_f8f6f4 v[96:99], v[138:145], v[48:55], v[96:99]
	v_mfma_f32_16x16x128_f8f6f4 v[92:95], v[130:137], v[162:169], v[92:95]
	v_mfma_f32_16x16x128_f8f6f4 v[88:91], v[138:145], v[162:169], v[88:91]
	v_mfma_f32_16x16x128_f8f6f4 v[84:87], v[130:137], v[196:203], v[84:87]
	v_mfma_f32_16x16x128_f8f6f4 v[80:83], v[138:145], v[196:203], v[80:83]
	v_mfma_f32_16x16x128_f8f6f4 v[76:79], v[130:137], v[232:239], v[170:173]
	v_mfma_f32_16x16x128_f8f6f4 v[72:75], v[138:145], v[232:239], v[188:191]
	s_setprio 0
	s_setprio 1
	v_mfma_f32_16x16x128_f8f6f4 v[68:71], v[146:153], v[48:55], v[248:251]
	v_mfma_f32_16x16x128_f8f6f4 v[64:67], v[154:161], v[48:55], v[204:207]
	v_mfma_f32_16x16x128_f8f6f4 v[60:63], v[146:153], v[162:169], v[208:211]
	v_mfma_f32_16x16x128_f8f6f4 v[56:59], v[154:161], v[162:169], v[212:215]
	v_mfma_f32_16x16x128_f8f6f4 v[52:55], v[146:153], v[196:203], v[216:219]
	v_mfma_f32_16x16x128_f8f6f4 v[48:51], v[154:161], v[196:203], v[240:243]
	v_mfma_f32_16x16x128_f8f6f4 v[40:43], v[146:153], v[232:239], v[40:43]
	v_mfma_f32_16x16x128_f8f6f4 v[32:35], v[154:161], v[232:239], v[32:35]
	s_setprio 0
	s_barrier
	v_mov_b32_e32 v185, v177
	ds_read_b128 v[162:165], v227 offset:49152
	ds_read_b128 v[196:199], v227 offset:51200
	ds_read_b128 v[166:169], v228 offset:49152
	ds_read_b128 v[200:203], v228 offset:51200
	ds_read_b128 v[232:235], v227 offset:53248
	ds_read_b128 v[240:243], v227 offset:55296
	ds_read_b128 v[236:239], v228 offset:53248
	ds_read_b128 v[244:247], v228 offset:55296
	s_add_i32 s43, s43, s5
	v_lshl_add_u64 v[128:129], s[40:41], 0, v[184:185]
	v_lshl_add_u64 v[128:129], v[128:129], 0, s[14:15]
	s_mov_b32 m0, s43
	v_mov_b32_e32 v179, v177
	global_load_lds_dwordx4 v[128:129], off
	s_add_i32 m0, s43, 0x2000
	v_mov_b32_e32 v181, v177
	v_lshl_add_u64 v[128:129], s[40:41], 0, v[178:179]
	s_add_u32 s40, s40, 0x4080
	v_lshl_add_u64 v[128:129], v[128:129], 0, s[14:15]
	s_addc_u32 s41, s41, 0
	s_add_i32 s43, s75, s5
	global_load_lds_dwordx4 v[128:129], off
	s_mov_b32 m0, s43
	v_mov_b32_e32 v183, v177
	global_load_lds_dwordx4 v184, s[40:41]
	s_add_i32 m0, s43, 0x2000
	s_nop 0
	global_load_lds_dwordx4 v178, s[40:41]
	s_mov_b32 m0, s62
	v_lshl_add_u64 v[128:129], s[38:39], 0, v[180:181]
	v_lshl_add_u64 v[128:129], v[128:129], 0, s[14:15]
	global_load_lds_dwordx4 v[128:129], off
	s_mov_b32 m0, s63
	v_lshl_add_u64 v[128:129], s[38:39], 0, v[182:183]
	v_lshl_add_u64 v[128:129], v[128:129], 0, s[14:15]
	global_load_lds_dwordx4 v[128:129], off
	s_waitcnt vmcnt(8)
	s_waitcnt lgkmcnt(0)
	s_barrier
	s_setprio 1
	s_waitcnt lgkmcnt(0)
	v_mfma_f32_16x16x128_f8f6f4 v[44:47], v[130:137], v[162:169], v[44:47]
	v_mfma_f32_16x16x128_f8f6f4 v[36:39], v[138:145], v[162:169], v[36:39]
	v_mfma_f32_16x16x128_f8f6f4 v[28:31], v[130:137], v[196:203], v[28:31]
	v_mfma_f32_16x16x128_f8f6f4 v[24:27], v[138:145], v[196:203], v[24:27]
	v_mfma_f32_16x16x128_f8f6f4 v[20:23], v[130:137], v[232:239], v[20:23]
	v_mfma_f32_16x16x128_f8f6f4 v[16:19], v[138:145], v[232:239], v[16:19]
	v_mfma_f32_16x16x128_f8f6f4 v[12:15], v[130:137], v[240:247], v[12:15]
	v_mfma_f32_16x16x128_f8f6f4 v[8:11], v[138:145], v[240:247], v[8:11]
	s_setprio 0
	s_setprio 1
	v_mfma_f32_16x16x128_f8f6f4 v[4:7], v[146:153], v[162:169], v[4:7]
	v_mfma_f32_16x16x128_f8f6f4 v[0:3], v[154:161], v[162:169], v[0:3]
	v_mfma_f32_16x16x128_f8f6f4 v[104:107], v[146:153], v[196:203], v[104:107]
	v_mfma_f32_16x16x128_f8f6f4 v[108:111], v[154:161], v[196:203], v[108:111]
	v_mfma_f32_16x16x128_f8f6f4 v[112:115], v[146:153], v[232:239], v[112:115]
	v_mfma_f32_16x16x128_f8f6f4 v[116:119], v[154:161], v[232:239], v[116:119]
	v_mfma_f32_16x16x128_f8f6f4 v[120:123], v[146:153], v[240:247], v[120:123]
	v_mfma_f32_16x16x128_f8f6f4 v[124:127], v[154:161], v[240:247], v[124:127]
	s_setprio 0
	s_barrier
	s_add_i32 s42, s42, 2
	s_add_u32 s36, s36, 0x100
	s_addc_u32 s37, s37, 0
	s_branch .LBB0_912
.LBB0_911:
	s_add_u32 s76, s10, s36
	v_add_u32_e32 v134, s67, v194
	v_add_u32_e32 v142, s67, v195
	v_add_u32_e32 v150, s68, v194
	v_add_u32_e32 v158, s68, v195
	s_addc_u32 s77, s11, s37
	ds_read_b128 v[130:133], v134
	ds_read_b128 v[138:141], v134 offset:2048
	ds_read_b128 v[134:137], v142
	ds_read_b128 v[142:145], v142 offset:2048
	ds_read_b128 v[146:149], v150
	ds_read_b128 v[154:157], v150 offset:2048
	ds_read_b128 v[150:153], v158
	ds_read_b128 v[158:161], v158 offset:2048
	s_add_u32 s43, s76, 0x36000100
	s_addc_u32 s75, s77, 0
	s_and_b64 s[38:39], s[40:41], exec
	s_cselect_b32 s39, s13, s75
	s_cselect_b32 s38, s12, s43
	s_add_u32 s43, s25, s36
	s_addc_u32 s75, s27, s37
	s_and_b64 s[40:41], s[40:41], exec
	s_cselect_b32 s41, s31, s75
	s_cselect_b32 s40, s30, s43
	ds_read_b128 v[162:165], v227
	ds_read_b128 v[232:235], v227 offset:2048
	ds_read_b128 v[166:169], v228
	ds_read_b128 v[236:239], v228 offset:2048
	ds_read_b128 v[240:243], v227 offset:4096
	ds_read_b128 v[196:199], v227 offset:6144
	ds_read_b128 v[244:247], v228 offset:4096
	ds_read_b128 v[200:203], v228 offset:6144
	s_add_i32 m0, s50, 0xc000
	v_lshl_add_u64 v[170:171], s[76:77], 0, v[176:177]
	v_lshl_add_u64 v[170:171], v[170:171], 0, s[16:17]
	v_mov_b32_e32 v187, v177
	global_load_lds_dwordx4 v[170:171], off
	s_add_i32 m0, s50, 0xe000
	v_lshl_add_u64 v[170:171], s[76:77], 0, v[186:187]
	v_lshl_add_u64 v[170:171], v[170:171], 0, s[16:17]
	global_load_lds_dwordx4 v[170:171], off
	s_waitcnt vmcnt(8)
	s_waitcnt lgkmcnt(0)
	s_barrier
	s_setprio 1
	s_waitcnt lgkmcnt(0)
	v_mfma_f32_16x16x128_f8f6f4 v[100:103], v[130:137], v[162:169], v[100:103]
	v_mfma_f32_16x16x128_f8f6f4 v[96:99], v[138:145], v[162:169], v[96:99]
	v_mfma_f32_16x16x128_f8f6f4 v[92:95], v[130:137], v[232:239], v[92:95]
	v_mfma_f32_16x16x128_f8f6f4 v[88:91], v[138:145], v[232:239], v[88:91]
	v_mfma_f32_16x16x128_f8f6f4 v[84:87], v[130:137], v[240:247], v[84:87]
	v_mfma_f32_16x16x128_f8f6f4 v[80:83], v[138:145], v[240:247], v[80:83]
	v_mfma_f32_16x16x128_f8f6f4 v[170:173], v[130:137], v[196:203], v[76:79]
	v_mfma_f32_16x16x128_f8f6f4 v[188:191], v[138:145], v[196:203], v[72:75]
	s_setprio 0
	s_setprio 1
	v_mfma_f32_16x16x128_f8f6f4 v[40:43], v[146:153], v[196:203], v[40:43]
	v_mfma_f32_16x16x128_f8f6f4 v[32:35], v[154:161], v[196:203], v[32:35]
	v_mfma_f32_16x16x128_f8f6f4 v[248:251], v[146:153], v[162:169], v[68:71]
	v_mfma_f32_16x16x128_f8f6f4 v[204:207], v[154:161], v[162:169], v[64:67]
	v_mfma_f32_16x16x128_f8f6f4 v[208:211], v[146:153], v[232:239], v[60:63]
	v_mfma_f32_16x16x128_f8f6f4 v[212:215], v[154:161], v[232:239], v[56:59]
	v_mfma_f32_16x16x128_f8f6f4 v[216:219], v[146:153], v[240:247], v[52:55]
	v_mfma_f32_16x16x128_f8f6f4 v[240:243], v[154:161], v[240:247], v[48:51]
	s_setprio 0
	s_barrier
	s_add_i32 s43, s67, s5
	s_mov_b32 m0, s43
	s_nop 2
	ds_read_b128 v[48:51], v227 offset:16384
	ds_read_b128 v[56:59], v227 offset:18432
	ds_read_b128 v[52:55], v228 offset:16384
	ds_read_b128 v[60:63], v228 offset:18432
	ds_read_b128 v[64:67], v227 offset:20480
	ds_read_b128 v[72:75], v227 offset:22528
	ds_read_b128 v[68:71], v228 offset:20480
	ds_read_b128 v[76:79], v228 offset:22528
	s_nop 0
	global_load_lds_dwordx4 v184, s[40:41]
	s_add_i32 m0, s43, 0x2000
	s_add_u32 s76, s40, 0x4000
	s_addc_u32 s77, s41, 0
	s_add_i32 s43, s68, s5
	s_nop 0
	global_load_lds_dwordx4 v178, s[40:41]
	s_mov_b32 m0, s43
	s_nop 0
	global_load_lds_dwordx4 v184, s[76:77]
	s_add_i32 m0, s43, 0x2000
	s_nop 0
	global_load_lds_dwordx4 v178, s[76:77]
	s_waitcnt vmcnt(6)
	s_waitcnt lgkmcnt(0)
	s_barrier
	s_setprio 1
	s_waitcnt lgkmcnt(0)
	v_mfma_f32_16x16x128_f8f6f4 v[44:47], v[130:137], v[48:55], v[44:47]
	v_mfma_f32_16x16x128_f8f6f4 v[36:39], v[138:145], v[48:55], v[36:39]
	v_mfma_f32_16x16x128_f8f6f4 v[28:31], v[130:137], v[56:63], v[28:31]
	v_mfma_f32_16x16x128_f8f6f4 v[24:27], v[138:145], v[56:63], v[24:27]
	v_mfma_f32_16x16x128_f8f6f4 v[20:23], v[130:137], v[64:71], v[20:23]
	v_mfma_f32_16x16x128_f8f6f4 v[16:19], v[138:145], v[64:71], v[16:19]
	v_mfma_f32_16x16x128_f8f6f4 v[12:15], v[130:137], v[72:79], v[12:15]
	v_mfma_f32_16x16x128_f8f6f4 v[8:11], v[138:145], v[72:79], v[8:11]
	s_setprio 0
	s_setprio 1
	v_mfma_f32_16x16x128_f8f6f4 v[4:7], v[146:153], v[48:55], v[4:7]
	v_mfma_f32_16x16x128_f8f6f4 v[0:3], v[154:161], v[48:55], v[0:3]
	v_mfma_f32_16x16x128_f8f6f4 v[104:107], v[146:153], v[56:63], v[104:107]
	v_mfma_f32_16x16x128_f8f6f4 v[108:111], v[154:161], v[56:63], v[108:111]
	v_mfma_f32_16x16x128_f8f6f4 v[112:115], v[146:153], v[64:71], v[112:115]
	v_mfma_f32_16x16x128_f8f6f4 v[116:119], v[154:161], v[64:71], v[116:119]
	v_mfma_f32_16x16x128_f8f6f4 v[120:123], v[146:153], v[72:79], v[120:123]
	v_mfma_f32_16x16x128_f8f6f4 v[124:127], v[154:161], v[72:79], v[124:127]
	s_setprio 0
	s_barrier
	s_add_i32 s43, 0, 0x18000
	v_add_u32_e32 v48, s43, v194
	s_add_i32 s75, 0, 0x1c000
	v_add_u32_e32 v49, s43, v195
	ds_read_b128 v[130:133], v48
	ds_read_b128 v[138:141], v48 offset:2048
	ds_read_b128 v[134:137], v49
	ds_read_b128 v[142:145], v49 offset:2048
	v_add_u32_e32 v48, s75, v194
	v_add_u32_e32 v49, s75, v195
	ds_read_b128 v[146:149], v48
	ds_read_b128 v[154:157], v48 offset:2048
	ds_read_b128 v[150:153], v49
	ds_read_b128 v[158:161], v49 offset:2048
	s_mov_b32 m0, s52
	v_mov_b32_e32 v176, v129
	ds_read_b128 v[48:51], v227 offset:32768
	ds_read_b128 v[162:165], v227 offset:34816
	ds_read_b128 v[52:55], v228 offset:32768
	ds_read_b128 v[166:169], v228 offset:34816
	ds_read_b128 v[196:199], v227 offset:36864
	ds_read_b128 v[232:235], v227 offset:38912
	ds_read_b128 v[200:203], v228 offset:36864
	ds_read_b128 v[236:239], v228 offset:38912
	s_mov_b32 m0, s50
	s_nop 0
	global_load_lds_dwordx4 v180, s[38:39]
	s_mov_b32 m0, s51
	s_nop 0
	global_load_lds_dwordx4 v182, s[38:39]
	s_mov_b32 m0, s52
	v_mov_b32_e32 v186, v128
	global_load_lds_dwordx4 v176, s[38:39]
	s_mov_b32 m0, s53
	s_nop 0
	global_load_lds_dwordx4 v186, s[38:39]
	s_waitcnt vmcnt(8)
	s_waitcnt lgkmcnt(0)
	s_barrier
	s_setprio 1
	s_waitcnt lgkmcnt(0)
	v_mfma_f32_16x16x128_f8f6f4 v[100:103], v[130:137], v[48:55], v[100:103]
	v_mfma_f32_16x16x128_f8f6f4 v[96:99], v[138:145], v[48:55], v[96:99]
	v_mfma_f32_16x16x128_f8f6f4 v[92:95], v[130:137], v[162:169], v[92:95]
	v_mfma_f32_16x16x128_f8f6f4 v[88:91], v[138:145], v[162:169], v[88:91]
	v_mfma_f32_16x16x128_f8f6f4 v[84:87], v[130:137], v[196:203], v[84:87]
	v_mfma_f32_16x16x128_f8f6f4 v[80:83], v[138:145], v[196:203], v[80:83]
	v_mfma_f32_16x16x128_f8f6f4 v[76:79], v[130:137], v[232:239], v[170:173]
	v_mfma_f32_16x16x128_f8f6f4 v[72:75], v[138:145], v[232:239], v[188:191]
	s_setprio 0
	s_setprio 1
	v_mfma_f32_16x16x128_f8f6f4 v[68:71], v[146:153], v[48:55], v[248:251]
	v_mfma_f32_16x16x128_f8f6f4 v[64:67], v[154:161], v[48:55], v[204:207]
	v_mfma_f32_16x16x128_f8f6f4 v[60:63], v[146:153], v[162:169], v[208:211]
	v_mfma_f32_16x16x128_f8f6f4 v[56:59], v[154:161], v[162:169], v[212:215]
	v_mfma_f32_16x16x128_f8f6f4 v[52:55], v[146:153], v[196:203], v[216:219]
	v_mfma_f32_16x16x128_f8f6f4 v[48:51], v[154:161], v[196:203], v[240:243]
	v_mfma_f32_16x16x128_f8f6f4 v[40:43], v[146:153], v[232:239], v[40:43]
	v_mfma_f32_16x16x128_f8f6f4 v[32:35], v[154:161], v[232:239], v[32:35]
	s_setprio 0
	s_barrier
	v_mov_b32_e32 v185, v177
	ds_read_b128 v[162:165], v227 offset:49152
	ds_read_b128 v[196:199], v227 offset:51200
	ds_read_b128 v[166:169], v228 offset:49152
	ds_read_b128 v[200:203], v228 offset:51200
	ds_read_b128 v[232:235], v227 offset:53248
	ds_read_b128 v[240:243], v227 offset:55296
	ds_read_b128 v[236:239], v228 offset:53248
	ds_read_b128 v[244:247], v228 offset:55296
	s_add_i32 s43, s43, s5
	v_lshl_add_u64 v[128:129], s[40:41], 0, v[184:185]
	v_lshl_add_u64 v[128:129], v[128:129], 0, s[14:15]
	s_mov_b32 m0, s43
	v_mov_b32_e32 v179, v177
	global_load_lds_dwordx4 v[128:129], off
	s_add_i32 m0, s43, 0x2000
	v_mov_b32_e32 v181, v177
	v_lshl_add_u64 v[128:129], s[40:41], 0, v[178:179]
	s_add_u32 s40, s40, 0x4080
	v_lshl_add_u64 v[128:129], v[128:129], 0, s[14:15]
	s_addc_u32 s41, s41, 0
	s_add_i32 s43, s75, s5
	global_load_lds_dwordx4 v[128:129], off
	s_mov_b32 m0, s43
	v_mov_b32_e32 v183, v177
	global_load_lds_dwordx4 v184, s[40:41]
	s_add_i32 m0, s43, 0x2000
	s_nop 0
	global_load_lds_dwordx4 v178, s[40:41]
	s_mov_b32 m0, s62
	v_lshl_add_u64 v[128:129], s[38:39], 0, v[180:181]
	v_lshl_add_u64 v[128:129], v[128:129], 0, s[14:15]
	global_load_lds_dwordx4 v[128:129], off
	s_mov_b32 m0, s63
	v_lshl_add_u64 v[128:129], s[38:39], 0, v[182:183]
	v_lshl_add_u64 v[128:129], v[128:129], 0, s[14:15]
	global_load_lds_dwordx4 v[128:129], off
	s_waitcnt vmcnt(8)
	s_waitcnt lgkmcnt(0)
	s_barrier
	s_setprio 1
	s_waitcnt lgkmcnt(0)
	v_mfma_f32_16x16x128_f8f6f4 v[44:47], v[130:137], v[162:169], v[44:47]
	v_mfma_f32_16x16x128_f8f6f4 v[36:39], v[138:145], v[162:169], v[36:39]
	v_mfma_f32_16x16x128_f8f6f4 v[28:31], v[130:137], v[196:203], v[28:31]
	v_mfma_f32_16x16x128_f8f6f4 v[24:27], v[138:145], v[196:203], v[24:27]
	v_mfma_f32_16x16x128_f8f6f4 v[20:23], v[130:137], v[232:239], v[20:23]
	v_mfma_f32_16x16x128_f8f6f4 v[16:19], v[138:145], v[232:239], v[16:19]
	v_mfma_f32_16x16x128_f8f6f4 v[12:15], v[130:137], v[240:247], v[12:15]
	v_mfma_f32_16x16x128_f8f6f4 v[8:11], v[138:145], v[240:247], v[8:11]
	s_setprio 0
	s_setprio 1
	v_mfma_f32_16x16x128_f8f6f4 v[4:7], v[146:153], v[162:169], v[4:7]
	v_mfma_f32_16x16x128_f8f6f4 v[0:3], v[154:161], v[162:169], v[0:3]
	v_mfma_f32_16x16x128_f8f6f4 v[104:107], v[146:153], v[196:203], v[104:107]
	v_mfma_f32_16x16x128_f8f6f4 v[108:111], v[154:161], v[196:203], v[108:111]
	v_mfma_f32_16x16x128_f8f6f4 v[112:115], v[146:153], v[232:239], v[112:115]
	v_mfma_f32_16x16x128_f8f6f4 v[116:119], v[154:161], v[232:239], v[116:119]
	v_mfma_f32_16x16x128_f8f6f4 v[120:123], v[146:153], v[240:247], v[120:123]
	v_mfma_f32_16x16x128_f8f6f4 v[124:127], v[154:161], v[240:247], v[124:127]
	s_setprio 0
	s_barrier
	s_add_i32 s42, s42, 2
	s_add_u32 s36, s36, 0x100
	s_addc_u32 s37, s37, 0
	s_cmp_gt_u32 s42, 13
	s_cbranch_scc1 .LBB0_914

.LBB0_1008:
	s_add_u32 s5, s38, 0x100
	s_addc_u32 s27, s39, 0
	s_lshl_b32 s44, s61, 8
	s_lshl_b32 s29, s61, 19
	s_bitset1_b32 s44, 7
	s_mov_b32 s45, -2
	s_mov_b64 s[38:39], 0
	s_cmp_eq_u32 s45, 12
	s_cselect_b64 s[42:43], -1, 0
	s_and_b64 s[40:41], s[36:37], s[42:43]
	s_andn2_b64 vcc, exec, s[40:41]
	v_mov_b32_e32 v131, v138
	v_mov_b32_e32 v133, v128
	v_add_u32_e32 v135, s58, v142
	s_add_u32 s64, s6, s38
	v_add_u32_e32 v137, s58, v143
	ds_read_b128 v[178:181], v135
	ds_read_b128 v[186:189], v135 offset:2048
	ds_read_b128 v[182:185], v137
	ds_read_b128 v[190:193], v137 offset:2048
	v_add_u32_e32 v135, s59, v142
	s_addc_u32 s65, s7, s39
	v_add_u32_e32 v137, s59, v143
	ds_read_b128 v[194:197], v135
	ds_read_b128 v[202:205], v135 offset:2048
	ds_read_b128 v[198:201], v137
	ds_read_b128 v[206:209], v137 offset:2048
	s_add_u32 s66, s64, 0x5e000100
	s_addc_u32 s67, s65, 0
	s_and_b64 s[40:41], s[42:43], exec
	s_cselect_b32 s41, s11, s67
	s_cselect_b32 s40, s10, s66
	s_add_u32 s66, s5, s38
	s_addc_u32 s67, s27, s39
	s_and_b64 s[42:43], s[42:43], exec
	s_cselect_b32 s43, s35, s67
	s_cselect_b32 s42, s34, s66
	ds_read_b128 v[210:213], v175
	ds_read_b128 v[218:221], v175 offset:2048
	ds_read_b128 v[214:217], v176
	ds_read_b128 v[222:225], v176 offset:2048
	ds_read_b128 v[226:229], v175 offset:4096
	ds_read_b128 v[234:237], v175 offset:6144
	ds_read_b128 v[230:233], v176 offset:4096
	ds_read_b128 v[238:241], v176 offset:6144
	s_add_i32 m0, s1, 0xc000
	v_lshl_add_u64 v[140:141], s[64:65], 0, v[128:129]
	v_lshl_add_u64 v[140:141], v[140:141], 0, s[16:17]
	global_load_lds_dwordx4 v[140:141], off
	v_mov_b32_e32 v139, v129
	v_lshl_add_u64 v[138:139], s[64:65], 0, v[138:139]
	v_lshl_add_u64 v[138:139], v[138:139], 0, s[16:17]
	s_add_i32 m0, s1, 0xe000
	s_nop 0
	global_load_lds_dwordx4 v[138:139], off
	s_waitcnt vmcnt(8)
	s_waitcnt lgkmcnt(0)
	s_barrier
	s_setprio 1
	s_waitcnt lgkmcnt(0)
	v_mfma_f32_16x16x128_f8f6f4 v[100:103], v[178:185], v[210:217], 0
	v_mfma_f32_16x16x128_f8f6f4 v[96:99], v[186:193], v[210:217], 0
	v_mfma_f32_16x16x128_f8f6f4 v[92:95], v[178:185], v[218:225], 0
	v_mfma_f32_16x16x128_f8f6f4 v[88:91], v[186:193], v[218:225], 0
	v_mfma_f32_16x16x128_f8f6f4 v[84:87], v[178:185], v[226:233], 0
	v_mfma_f32_16x16x128_f8f6f4 v[80:83], v[186:193], v[226:233], 0
	v_mfma_f32_16x16x128_f8f6f4 v[242:245], v[178:185], v[234:241], 0
	v_mfma_f32_16x16x128_f8f6f4 v[246:249], v[186:193], v[234:241], 0
	s_setprio 0
	s_setprio 1
	v_mfma_f32_16x16x128_f8f6f4 v[40:43], v[194:201], v[234:241], 0
	v_mfma_f32_16x16x128_f8f6f4 v[32:35], v[202:209], v[234:241], 0
	v_mfma_f32_16x16x128_f8f6f4 v[250:253], v[194:201], v[210:217], 0
	v_mfma_f32_16x16x128_f8f6f4 v[144:147], v[202:209], v[210:217], 0
	v_mfma_f32_16x16x128_f8f6f4 v[148:151], v[194:201], v[218:225], 0
	v_mfma_f32_16x16x128_f8f6f4 v[152:155], v[202:209], v[218:225], 0
	v_mfma_f32_16x16x128_f8f6f4 v[156:159], v[194:201], v[226:233], 0
	v_mfma_f32_16x16x128_f8f6f4 v[160:163], v[202:209], v[226:233], 0
	s_setprio 0
	s_barrier
	s_add_i32 s64, s58, s48
	s_mov_b32 m0, s64
	s_nop 2
	ds_read_b128 v[48:51], v175 offset:16384
	ds_read_b128 v[56:59], v175 offset:18432
	ds_read_b128 v[52:55], v176 offset:16384
	ds_read_b128 v[60:63], v176 offset:18432
	ds_read_b128 v[64:67], v175 offset:20480
	ds_read_b128 v[72:75], v175 offset:22528
	ds_read_b128 v[68:71], v176 offset:20480
	ds_read_b128 v[76:79], v176 offset:22528
	s_nop 0
	global_load_lds_dwordx4 v136, s[42:43]
	s_add_i32 m0, s64, 0x2000
	s_add_u32 s64, s42, 0x4000
	s_addc_u32 s65, s43, 0
	s_add_i32 s66, s59, s48
	s_nop 0
	global_load_lds_dwordx4 v130, s[42:43]
	s_mov_b32 m0, s66
	s_nop 0
	global_load_lds_dwordx4 v136, s[64:65]
	s_add_i32 m0, s66, 0x2000
	s_nop 0
	global_load_lds_dwordx4 v130, s[64:65]
	s_waitcnt vmcnt(6)
	s_waitcnt lgkmcnt(0)
	s_barrier
	s_setprio 1
	s_waitcnt lgkmcnt(0)
	v_mfma_f32_16x16x128_f8f6f4 v[44:47], v[178:185], v[48:55], 0
	v_mfma_f32_16x16x128_f8f6f4 v[36:39], v[186:193], v[48:55], 0
	v_mfma_f32_16x16x128_f8f6f4 v[28:31], v[178:185], v[56:63], 0
	v_mfma_f32_16x16x128_f8f6f4 v[24:27], v[186:193], v[56:63], 0
	v_mfma_f32_16x16x128_f8f6f4 v[20:23], v[178:185], v[64:71], 0
	v_mfma_f32_16x16x128_f8f6f4 v[16:19], v[186:193], v[64:71], 0
	v_mfma_f32_16x16x128_f8f6f4 v[12:15], v[178:185], v[72:79], 0
	v_mfma_f32_16x16x128_f8f6f4 v[8:11], v[186:193], v[72:79], 0
	s_setprio 0
	s_setprio 1
	v_mfma_f32_16x16x128_f8f6f4 v[4:7], v[194:201], v[48:55], 0
	v_mfma_f32_16x16x128_f8f6f4 v[0:3], v[202:209], v[48:55], 0
	v_mfma_f32_16x16x128_f8f6f4 v[104:107], v[194:201], v[56:63], 0
	v_mfma_f32_16x16x128_f8f6f4 v[108:111], v[202:209], v[56:63], 0
	v_mfma_f32_16x16x128_f8f6f4 v[112:115], v[194:201], v[64:71], 0
	v_mfma_f32_16x16x128_f8f6f4 v[116:119], v[202:209], v[64:71], 0
	v_mfma_f32_16x16x128_f8f6f4 v[120:123], v[194:201], v[72:79], 0
	v_mfma_f32_16x16x128_f8f6f4 v[124:127], v[202:209], v[72:79], 0
	s_setprio 0
	s_barrier
	s_add_i32 s64, 0, 0x18000
	v_add_u32_e32 v48, s64, v142
	s_add_i32 s65, 0, 0x1c000
	v_add_u32_e32 v49, s64, v143
	ds_read_b128 v[178:181], v48
	ds_read_b128 v[186:189], v48 offset:2048
	ds_read_b128 v[182:185], v49
	ds_read_b128 v[190:193], v49 offset:2048
	v_add_u32_e32 v48, s65, v142
	v_add_u32_e32 v49, s65, v143
	ds_read_b128 v[194:197], v48
	ds_read_b128 v[202:205], v48 offset:2048
	ds_read_b128 v[198:201], v49
	ds_read_b128 v[206:209], v49 offset:2048
	s_mov_b32 m0, s50
	v_mov_b32_e32 v128, v133
	ds_read_b128 v[48:51], v175 offset:32768
	ds_read_b128 v[210:213], v175 offset:34816
	ds_read_b128 v[52:55], v176 offset:32768
	ds_read_b128 v[214:217], v176 offset:34816
	ds_read_b128 v[218:221], v175 offset:36864
	ds_read_b128 v[226:229], v175 offset:38912
	ds_read_b128 v[222:225], v176 offset:36864
	ds_read_b128 v[230:233], v176 offset:38912
	s_mov_b32 m0, s1
	s_nop 0
	global_load_lds_dwordx4 v132, s[40:41]
	s_mov_b32 m0, s49
	s_nop 0
	global_load_lds_dwordx4 v134, s[40:41]
	s_mov_b32 m0, s50
	v_mov_b32_e32 v138, v131
	global_load_lds_dwordx4 v128, s[40:41]
	s_mov_b32 m0, s51
	s_nop 0
	global_load_lds_dwordx4 v138, s[40:41]
	s_waitcnt vmcnt(8)
	s_waitcnt lgkmcnt(0)
	s_barrier
	s_setprio 1
	s_waitcnt lgkmcnt(0)
	v_mfma_f32_16x16x128_f8f6f4 v[100:103], v[178:185], v[48:55], v[100:103]
	v_mfma_f32_16x16x128_f8f6f4 v[96:99], v[186:193], v[48:55], v[96:99]
	v_mfma_f32_16x16x128_f8f6f4 v[92:95], v[178:185], v[210:217], v[92:95]
	v_mfma_f32_16x16x128_f8f6f4 v[88:91], v[186:193], v[210:217], v[88:91]
	v_mfma_f32_16x16x128_f8f6f4 v[84:87], v[178:185], v[218:225], v[84:87]
	v_mfma_f32_16x16x128_f8f6f4 v[80:83], v[186:193], v[218:225], v[80:83]
	v_mfma_f32_16x16x128_f8f6f4 v[76:79], v[178:185], v[226:233], v[242:245]
	v_mfma_f32_16x16x128_f8f6f4 v[72:75], v[186:193], v[226:233], v[246:249]
	s_setprio 0
	s_setprio 1
	v_mfma_f32_16x16x128_f8f6f4 v[68:71], v[194:201], v[48:55], v[250:253]
	v_mfma_f32_16x16x128_f8f6f4 v[64:67], v[202:209], v[48:55], v[144:147]
	v_mfma_f32_16x16x128_f8f6f4 v[60:63], v[194:201], v[210:217], v[148:151]
	v_mfma_f32_16x16x128_f8f6f4 v[56:59], v[202:209], v[210:217], v[152:155]
	v_mfma_f32_16x16x128_f8f6f4 v[52:55], v[194:201], v[218:225], v[156:159]
	v_mfma_f32_16x16x128_f8f6f4 v[48:51], v[202:209], v[218:225], v[160:163]
	v_mfma_f32_16x16x128_f8f6f4 v[40:43], v[194:201], v[226:233], v[40:43]
	v_mfma_f32_16x16x128_f8f6f4 v[32:35], v[202:209], v[226:233], v[32:35]
	s_setprio 0
	s_barrier
	v_mov_b32_e32 v137, v129
	ds_read_b128 v[210:213], v175 offset:49152
	ds_read_b128 v[218:221], v175 offset:51200
	ds_read_b128 v[214:217], v176 offset:49152
	ds_read_b128 v[222:225], v176 offset:51200
	ds_read_b128 v[226:229], v175 offset:53248
	ds_read_b128 v[234:237], v175 offset:55296
	ds_read_b128 v[230:233], v176 offset:53248
	ds_read_b128 v[238:241], v176 offset:55296
	s_add_i32 s64, s64, s48
	v_lshl_add_u64 v[140:141], s[42:43], 0, v[136:137]
	v_lshl_add_u64 v[140:141], v[140:141], 0, s[14:15]
	s_mov_b32 m0, s64
	v_mov_b32_e32 v131, v129
	global_load_lds_dwordx4 v[140:141], off
	s_add_i32 m0, s64, 0x2000
	v_mov_b32_e32 v133, v129
	v_lshl_add_u64 v[140:141], s[42:43], 0, v[130:131]
	s_add_u32 s42, s42, 0x4080
	v_lshl_add_u64 v[140:141], v[140:141], 0, s[14:15]
	s_addc_u32 s43, s43, 0
	s_add_i32 s64, s65, s48
	global_load_lds_dwordx4 v[140:141], off
	s_mov_b32 m0, s64
	v_mov_b32_e32 v135, v129
	global_load_lds_dwordx4 v136, s[42:43]
	s_add_i32 m0, s64, 0x2000
	s_nop 0
	global_load_lds_dwordx4 v130, s[42:43]
	s_mov_b32 m0, s53
	v_lshl_add_u64 v[140:141], s[40:41], 0, v[132:133]
	v_lshl_add_u64 v[140:141], v[140:141], 0, s[14:15]
	global_load_lds_dwordx4 v[140:141], off
	s_mov_b32 m0, s54
	v_lshl_add_u64 v[140:141], s[40:41], 0, v[134:135]
	v_lshl_add_u64 v[140:141], v[140:141], 0, s[14:15]
	global_load_lds_dwordx4 v[140:141], off
	s_waitcnt vmcnt(8)
	s_waitcnt lgkmcnt(0)
	s_barrier
	s_setprio 1
	s_waitcnt lgkmcnt(0)
	v_mfma_f32_16x16x128_f8f6f4 v[44:47], v[178:185], v[210:217], v[44:47]
	v_mfma_f32_16x16x128_f8f6f4 v[36:39], v[186:193], v[210:217], v[36:39]
	v_mfma_f32_16x16x128_f8f6f4 v[28:31], v[178:185], v[218:225], v[28:31]
	v_mfma_f32_16x16x128_f8f6f4 v[24:27], v[186:193], v[218:225], v[24:27]
	v_mfma_f32_16x16x128_f8f6f4 v[20:23], v[178:185], v[226:233], v[20:23]
	v_mfma_f32_16x16x128_f8f6f4 v[16:19], v[186:193], v[226:233], v[16:19]
	v_mfma_f32_16x16x128_f8f6f4 v[12:15], v[178:185], v[234:241], v[12:15]
	v_mfma_f32_16x16x128_f8f6f4 v[8:11], v[186:193], v[234:241], v[8:11]
	s_setprio 0
	s_setprio 1
	v_mfma_f32_16x16x128_f8f6f4 v[4:7], v[194:201], v[210:217], v[4:7]
	v_mfma_f32_16x16x128_f8f6f4 v[0:3], v[202:209], v[210:217], v[0:3]
	v_mfma_f32_16x16x128_f8f6f4 v[104:107], v[194:201], v[218:225], v[104:107]
	v_mfma_f32_16x16x128_f8f6f4 v[108:111], v[202:209], v[218:225], v[108:111]
	v_mfma_f32_16x16x128_f8f6f4 v[112:115], v[194:201], v[226:233], v[112:115]
	v_mfma_f32_16x16x128_f8f6f4 v[116:119], v[202:209], v[226:233], v[116:119]
	v_mfma_f32_16x16x128_f8f6f4 v[120:123], v[194:201], v[234:241], v[120:123]
	v_mfma_f32_16x16x128_f8f6f4 v[124:127], v[202:209], v[234:241], v[124:127]
	s_setprio 0
	s_barrier
	s_add_i32 s45, s45, 2
	s_add_u32 s38, s38, 0x100
	s_addc_u32 s39, s39, 0
	s_branch .LBB0_1010
.LBB0_1009:
	v_add_u32_e32 v135, s58, v142
	s_add_u32 s64, s6, s38
	v_add_u32_e32 v137, s58, v143
	ds_read_b128 v[178:181], v135
	ds_read_b128 v[186:189], v135 offset:2048
	ds_read_b128 v[182:185], v137
	ds_read_b128 v[190:193], v137 offset:2048
	v_add_u32_e32 v135, s59, v142
	s_addc_u32 s65, s7, s39
	v_add_u32_e32 v137, s59, v143
	ds_read_b128 v[194:197], v135
	ds_read_b128 v[202:205], v135 offset:2048
	ds_read_b128 v[198:201], v137
	ds_read_b128 v[206:209], v137 offset:2048
	s_add_u32 s66, s64, 0x5e000100
	s_addc_u32 s67, s65, 0
	s_and_b64 s[40:41], s[42:43], exec
	s_cselect_b32 s41, s11, s67
	s_cselect_b32 s40, s10, s66
	s_add_u32 s66, s5, s38
	s_addc_u32 s67, s27, s39
	s_and_b64 s[42:43], s[42:43], exec
	s_cselect_b32 s43, s35, s67
	s_cselect_b32 s42, s34, s66
	ds_read_b128 v[210:213], v175
	ds_read_b128 v[218:221], v175 offset:2048
	ds_read_b128 v[214:217], v176
	ds_read_b128 v[222:225], v176 offset:2048
	ds_read_b128 v[226:229], v175 offset:4096
	ds_read_b128 v[234:237], v175 offset:6144
	ds_read_b128 v[230:233], v176 offset:4096
	ds_read_b128 v[238:241], v176 offset:6144
	s_add_i32 m0, s1, 0xc000
	v_lshl_add_u64 v[140:141], s[64:65], 0, v[128:129]
	v_lshl_add_u64 v[140:141], v[140:141], 0, s[16:17]
	global_load_lds_dwordx4 v[140:141], off
	v_mov_b32_e32 v139, v129
	v_lshl_add_u64 v[138:139], s[64:65], 0, v[138:139]
	v_lshl_add_u64 v[138:139], v[138:139], 0, s[16:17]
	s_add_i32 m0, s1, 0xe000
	s_nop 0
	global_load_lds_dwordx4 v[138:139], off
	s_waitcnt vmcnt(8)
	s_waitcnt lgkmcnt(0)
	s_barrier
	s_setprio 1
	s_waitcnt lgkmcnt(0)
	v_mfma_f32_16x16x128_f8f6f4 v[100:103], v[178:185], v[210:217], v[100:103]
	v_mfma_f32_16x16x128_f8f6f4 v[96:99], v[186:193], v[210:217], v[96:99]
	v_mfma_f32_16x16x128_f8f6f4 v[92:95], v[178:185], v[218:225], v[92:95]
	v_mfma_f32_16x16x128_f8f6f4 v[88:91], v[186:193], v[218:225], v[88:91]
	v_mfma_f32_16x16x128_f8f6f4 v[84:87], v[178:185], v[226:233], v[84:87]
	v_mfma_f32_16x16x128_f8f6f4 v[80:83], v[186:193], v[226:233], v[80:83]
	v_mfma_f32_16x16x128_f8f6f4 v[242:245], v[178:185], v[234:241], v[76:79]
	v_mfma_f32_16x16x128_f8f6f4 v[246:249], v[186:193], v[234:241], v[72:75]
	s_setprio 0
	s_setprio 1
	v_mfma_f32_16x16x128_f8f6f4 v[40:43], v[194:201], v[234:241], v[40:43]
	v_mfma_f32_16x16x128_f8f6f4 v[32:35], v[202:209], v[234:241], v[32:35]
	v_mfma_f32_16x16x128_f8f6f4 v[250:253], v[194:201], v[210:217], v[68:71]
	v_mfma_f32_16x16x128_f8f6f4 v[144:147], v[202:209], v[210:217], v[64:67]
	v_mfma_f32_16x16x128_f8f6f4 v[148:151], v[194:201], v[218:225], v[60:63]
	v_mfma_f32_16x16x128_f8f6f4 v[152:155], v[202:209], v[218:225], v[56:59]
	v_mfma_f32_16x16x128_f8f6f4 v[156:159], v[194:201], v[226:233], v[52:55]
	v_mfma_f32_16x16x128_f8f6f4 v[160:163], v[202:209], v[226:233], v[48:51]
	s_setprio 0
	s_barrier
	s_add_i32 s64, s58, s48
	s_mov_b32 m0, s64
	s_nop 2
	ds_read_b128 v[48:51], v175 offset:16384
	ds_read_b128 v[56:59], v175 offset:18432
	ds_read_b128 v[52:55], v176 offset:16384
	ds_read_b128 v[60:63], v176 offset:18432
	ds_read_b128 v[64:67], v175 offset:20480
	ds_read_b128 v[72:75], v175 offset:22528
	ds_read_b128 v[68:71], v176 offset:20480
	ds_read_b128 v[76:79], v176 offset:22528
	s_nop 0
	global_load_lds_dwordx4 v136, s[42:43]
	s_add_i32 m0, s64, 0x2000
	s_add_u32 s64, s42, 0x4000
	s_addc_u32 s65, s43, 0
	s_add_i32 s66, s59, s48
	s_nop 0
	global_load_lds_dwordx4 v130, s[42:43]
	s_mov_b32 m0, s66
	s_nop 0
	global_load_lds_dwordx4 v136, s[64:65]
	s_add_i32 m0, s66, 0x2000
	s_nop 0
	global_load_lds_dwordx4 v130, s[64:65]
	s_waitcnt vmcnt(6)
	s_waitcnt lgkmcnt(0)
	s_barrier
	s_setprio 1
	s_waitcnt lgkmcnt(0)
	v_mfma_f32_16x16x128_f8f6f4 v[44:47], v[178:185], v[48:55], v[44:47]
	v_mfma_f32_16x16x128_f8f6f4 v[36:39], v[186:193], v[48:55], v[36:39]
	v_mfma_f32_16x16x128_f8f6f4 v[28:31], v[178:185], v[56:63], v[28:31]
	v_mfma_f32_16x16x128_f8f6f4 v[24:27], v[186:193], v[56:63], v[24:27]
	v_mfma_f32_16x16x128_f8f6f4 v[20:23], v[178:185], v[64:71], v[20:23]
	v_mfma_f32_16x16x128_f8f6f4 v[16:19], v[186:193], v[64:71], v[16:19]
	v_mfma_f32_16x16x128_f8f6f4 v[12:15], v[178:185], v[72:79], v[12:15]
	v_mfma_f32_16x16x128_f8f6f4 v[8:11], v[186:193], v[72:79], v[8:11]
	s_setprio 0
	s_setprio 1
	v_mfma_f32_16x16x128_f8f6f4 v[4:7], v[194:201], v[48:55], v[4:7]
	v_mfma_f32_16x16x128_f8f6f4 v[0:3], v[202:209], v[48:55], v[0:3]
	v_mfma_f32_16x16x128_f8f6f4 v[104:107], v[194:201], v[56:63], v[104:107]
	v_mfma_f32_16x16x128_f8f6f4 v[108:111], v[202:209], v[56:63], v[108:111]
	v_mfma_f32_16x16x128_f8f6f4 v[112:115], v[194:201], v[64:71], v[112:115]
	v_mfma_f32_16x16x128_f8f6f4 v[116:119], v[202:209], v[64:71], v[116:119]
	v_mfma_f32_16x16x128_f8f6f4 v[120:123], v[194:201], v[72:79], v[120:123]
	v_mfma_f32_16x16x128_f8f6f4 v[124:127], v[202:209], v[72:79], v[124:127]
	s_setprio 0
	s_barrier
	s_add_i32 s64, 0, 0x18000
	v_add_u32_e32 v48, s64, v142
	s_add_i32 s65, 0, 0x1c000
	v_add_u32_e32 v49, s64, v143
	ds_read_b128 v[178:181], v48
	ds_read_b128 v[186:189], v48 offset:2048
	ds_read_b128 v[182:185], v49
	ds_read_b128 v[190:193], v49 offset:2048
	v_add_u32_e32 v48, s65, v142
	v_add_u32_e32 v49, s65, v143
	ds_read_b128 v[194:197], v48
	ds_read_b128 v[202:205], v48 offset:2048
	ds_read_b128 v[198:201], v49
	ds_read_b128 v[206:209], v49 offset:2048
	s_mov_b32 m0, s50
	v_mov_b32_e32 v128, v133
	ds_read_b128 v[48:51], v175 offset:32768
	ds_read_b128 v[210:213], v175 offset:34816
	ds_read_b128 v[52:55], v176 offset:32768
	ds_read_b128 v[214:217], v176 offset:34816
	ds_read_b128 v[218:221], v175 offset:36864
	ds_read_b128 v[226:229], v175 offset:38912
	ds_read_b128 v[222:225], v176 offset:36864
	ds_read_b128 v[230:233], v176 offset:38912
	s_mov_b32 m0, s1
	s_nop 0
	global_load_lds_dwordx4 v132, s[40:41]
	s_mov_b32 m0, s49
	s_nop 0
	global_load_lds_dwordx4 v134, s[40:41]
	s_mov_b32 m0, s50
	v_mov_b32_e32 v138, v131
	global_load_lds_dwordx4 v128, s[40:41]
	s_mov_b32 m0, s51
	s_nop 0
	global_load_lds_dwordx4 v138, s[40:41]
	s_waitcnt vmcnt(8)
	s_waitcnt lgkmcnt(0)
	s_barrier
	s_setprio 1
	s_waitcnt lgkmcnt(0)
	v_mfma_f32_16x16x128_f8f6f4 v[100:103], v[178:185], v[48:55], v[100:103]
	v_mfma_f32_16x16x128_f8f6f4 v[96:99], v[186:193], v[48:55], v[96:99]
	v_mfma_f32_16x16x128_f8f6f4 v[92:95], v[178:185], v[210:217], v[92:95]
	v_mfma_f32_16x16x128_f8f6f4 v[88:91], v[186:193], v[210:217], v[88:91]
	v_mfma_f32_16x16x128_f8f6f4 v[84:87], v[178:185], v[218:225], v[84:87]
	v_mfma_f32_16x16x128_f8f6f4 v[80:83], v[186:193], v[218:225], v[80:83]
	v_mfma_f32_16x16x128_f8f6f4 v[76:79], v[178:185], v[226:233], v[242:245]
	v_mfma_f32_16x16x128_f8f6f4 v[72:75], v[186:193], v[226:233], v[246:249]
	s_setprio 0
	s_setprio 1
	v_mfma_f32_16x16x128_f8f6f4 v[68:71], v[194:201], v[48:55], v[250:253]
	v_mfma_f32_16x16x128_f8f6f4 v[64:67], v[202:209], v[48:55], v[144:147]
	v_mfma_f32_16x16x128_f8f6f4 v[60:63], v[194:201], v[210:217], v[148:151]
	v_mfma_f32_16x16x128_f8f6f4 v[56:59], v[202:209], v[210:217], v[152:155]
	v_mfma_f32_16x16x128_f8f6f4 v[52:55], v[194:201], v[218:225], v[156:159]
	v_mfma_f32_16x16x128_f8f6f4 v[48:51], v[202:209], v[218:225], v[160:163]
	v_mfma_f32_16x16x128_f8f6f4 v[40:43], v[194:201], v[226:233], v[40:43]
	v_mfma_f32_16x16x128_f8f6f4 v[32:35], v[202:209], v[226:233], v[32:35]
	s_setprio 0
	s_barrier
	v_mov_b32_e32 v137, v129
	ds_read_b128 v[210:213], v175 offset:49152
	ds_read_b128 v[218:221], v175 offset:51200
	ds_read_b128 v[214:217], v176 offset:49152
	ds_read_b128 v[222:225], v176 offset:51200
	ds_read_b128 v[226:229], v175 offset:53248
	ds_read_b128 v[234:237], v175 offset:55296
	ds_read_b128 v[230:233], v176 offset:53248
	ds_read_b128 v[238:241], v176 offset:55296
	s_add_i32 s64, s64, s48
	v_lshl_add_u64 v[140:141], s[42:43], 0, v[136:137]
	v_lshl_add_u64 v[140:141], v[140:141], 0, s[14:15]
	s_mov_b32 m0, s64
	v_mov_b32_e32 v131, v129
	global_load_lds_dwordx4 v[140:141], off
	s_add_i32 m0, s64, 0x2000
	v_mov_b32_e32 v133, v129
	v_lshl_add_u64 v[140:141], s[42:43], 0, v[130:131]
	s_add_u32 s42, s42, 0x4080
	v_lshl_add_u64 v[140:141], v[140:141], 0, s[14:15]
	s_addc_u32 s43, s43, 0
	s_add_i32 s64, s65, s48
	global_load_lds_dwordx4 v[140:141], off
	s_mov_b32 m0, s64
	v_mov_b32_e32 v135, v129
	global_load_lds_dwordx4 v136, s[42:43]
	s_add_i32 m0, s64, 0x2000
	s_nop 0
	global_load_lds_dwordx4 v130, s[42:43]
	s_mov_b32 m0, s53
	v_lshl_add_u64 v[140:141], s[40:41], 0, v[132:133]
	v_lshl_add_u64 v[140:141], v[140:141], 0, s[14:15]
	global_load_lds_dwordx4 v[140:141], off
	s_mov_b32 m0, s54
	v_lshl_add_u64 v[140:141], s[40:41], 0, v[134:135]
	v_lshl_add_u64 v[140:141], v[140:141], 0, s[14:15]
	global_load_lds_dwordx4 v[140:141], off
	s_waitcnt vmcnt(8)
	s_waitcnt lgkmcnt(0)
	s_barrier
	s_setprio 1
	s_waitcnt lgkmcnt(0)
	v_mfma_f32_16x16x128_f8f6f4 v[44:47], v[178:185], v[210:217], v[44:47]
	v_mfma_f32_16x16x128_f8f6f4 v[36:39], v[186:193], v[210:217], v[36:39]
	v_mfma_f32_16x16x128_f8f6f4 v[28:31], v[178:185], v[218:225], v[28:31]
	v_mfma_f32_16x16x128_f8f6f4 v[24:27], v[186:193], v[218:225], v[24:27]
	v_mfma_f32_16x16x128_f8f6f4 v[20:23], v[178:185], v[226:233], v[20:23]
	v_mfma_f32_16x16x128_f8f6f4 v[16:19], v[186:193], v[226:233], v[16:19]
	v_mfma_f32_16x16x128_f8f6f4 v[12:15], v[178:185], v[234:241], v[12:15]
	v_mfma_f32_16x16x128_f8f6f4 v[8:11], v[186:193], v[234:241], v[8:11]
	s_setprio 0
	s_setprio 1
	v_mfma_f32_16x16x128_f8f6f4 v[4:7], v[194:201], v[210:217], v[4:7]
	v_mfma_f32_16x16x128_f8f6f4 v[0:3], v[202:209], v[210:217], v[0:3]
	v_mfma_f32_16x16x128_f8f6f4 v[104:107], v[194:201], v[218:225], v[104:107]
	v_mfma_f32_16x16x128_f8f6f4 v[108:111], v[202:209], v[218:225], v[108:111]
	v_mfma_f32_16x16x128_f8f6f4 v[112:115], v[194:201], v[226:233], v[112:115]
	v_mfma_f32_16x16x128_f8f6f4 v[116:119], v[202:209], v[226:233], v[116:119]
	v_mfma_f32_16x16x128_f8f6f4 v[120:123], v[194:201], v[234:241], v[120:123]
	v_mfma_f32_16x16x128_f8f6f4 v[124:127], v[202:209], v[234:241], v[124:127]
	s_setprio 0
	s_barrier
	s_add_i32 s45, s45, 2
	s_add_u32 s38, s38, 0x100
	s_addc_u32 s39, s39, 0
	s_cmp_gt_u32 s45, 13
	s_cbranch_scc1 .LBB0_1012
